# GDN step 4: zero block of the T images written with 8-byte LDS writes (8 instead of 64 16-bit writes on the two critical waves); plus all earlier changes
# speedup vs baseline: 1.0116x; 1.0060x over previous
.Lg4_s1done:
	s_waitcnt lgkmcnt(0)
	s_barrier
	s_lshr_b32 s1, s10, 2
	s_and_b32 s11, s10, 3
	v_lshrrev_b32_e32 v4, 5, v21
	v_and_b32_e32 v108, 31, v21
	s_mul_i32 s12, s1, 0x3000
	v_lshl_add_u32 v4, s11, 1, v4
	s_mul_i32 s13, s1, 0x4800
	s_add_i32 s12, s12, 0x1b000
	v_lshlrev_b32_e32 v5, 2, v108
	v_mul_u32_u24_e32 v6, 0x440, v4
	v_lshlrev_b32_e32 v7, 9, v4
	v_add3_u32 v8, v61, v5, s12
	s_add_i32 s24, s13, 0x2200
	v_add3_u32 v9, v61, v6, s24
	v_add_u32_e32 v10, v8, v7
	v_add3_u32 v11, v61, v7, s12
	ds_read_b32 v200, v8 offset:0
	ds_read_b32 v201, v8 offset:128
	ds_read_b32 v202, v8 offset:256
	ds_read_b32 v203, v8 offset:384
	ds_read_b32 v204, v8 offset:512
	ds_read_b32 v205, v8 offset:640
	ds_read_b32 v206, v8 offset:768
	ds_read_b32 v207, v8 offset:896
	ds_read_b32 v208, v8 offset:1024
	ds_read_b32 v209, v8 offset:1152
	ds_read_b32 v210, v8 offset:1280
	ds_read_b32 v211, v8 offset:1408
	ds_read_b32 v212, v8 offset:1536
	ds_read_b32 v213, v8 offset:1664
	ds_read_b32 v214, v8 offset:1792
	ds_read_b32 v215, v8 offset:1920
	ds_read_b32 v216, v8 offset:2048
	ds_read_b32 v217, v8 offset:2176
	ds_read_b32 v218, v8 offset:2304
	ds_read_b32 v219, v8 offset:2432
	ds_read_b32 v220, v8 offset:2560
	ds_read_b32 v221, v8 offset:2688
	ds_read_b32 v222, v8 offset:2816
	ds_read_b32 v223, v8 offset:2944
	ds_read_b32 v224, v8 offset:3072
	ds_read_b32 v225, v8 offset:3200
	ds_read_b32 v226, v8 offset:3328
	ds_read_b32 v227, v8 offset:3456
	ds_read_b32 v228, v8 offset:3584
	ds_read_b32 v229, v8 offset:3712
	ds_read_b32 v230, v8 offset:3840
	ds_read_b32 v231, v8 offset:3968
	ds_read_b128 v[136:139], v9 offset:0
	ds_read_b128 v[140:143], v9 offset:16
	ds_read_b128 v[144:147], v9 offset:32
	ds_read_b128 v[148:151], v9 offset:48
	ds_read_b128 v[152:155], v9 offset:64
	ds_read_b128 v[156:159], v9 offset:80
	ds_read_b128 v[160:163], v9 offset:96
	ds_read_b128 v[164:167], v9 offset:112
	s_waitcnt lgkmcnt(0)
	ds_read_b128 v[168:171], v9 offset:272
	ds_read_b128 v[172:175], v9 offset:288
	ds_read_b128 v[176:179], v9 offset:304
	ds_read_b128 v[180:183], v9 offset:320
	ds_read_b128 v[184:187], v9 offset:336
	ds_read_b128 v[188:191], v9 offset:352
	ds_read_b128 v[192:195], v9 offset:368
	ds_read_b128 v[196:199], v9 offset:384
	v_mul_f32_e32 v104, v136, v200
	v_mul_f32_e32 v105, v137, v201
	v_fmac_f32_e32 v104, v138, v202
	v_fmac_f32_e32 v105, v139, v203
	v_fmac_f32_e32 v104, v140, v204
	v_fmac_f32_e32 v105, v141, v205
	v_fmac_f32_e32 v104, v142, v206
	v_fmac_f32_e32 v105, v143, v207
	v_fmac_f32_e32 v104, v144, v208
	v_fmac_f32_e32 v105, v145, v209
	v_fmac_f32_e32 v104, v146, v210
	v_fmac_f32_e32 v105, v147, v211
	v_fmac_f32_e32 v104, v148, v212
	v_fmac_f32_e32 v105, v149, v213
	v_fmac_f32_e32 v104, v150, v214
	v_fmac_f32_e32 v105, v151, v215
	v_fmac_f32_e32 v104, v152, v216
	v_fmac_f32_e32 v105, v153, v217
	v_fmac_f32_e32 v104, v154, v218
	v_fmac_f32_e32 v105, v155, v219
	v_fmac_f32_e32 v104, v156, v220
	v_fmac_f32_e32 v105, v157, v221
	v_fmac_f32_e32 v104, v158, v222
	v_fmac_f32_e32 v105, v159, v223
	v_fmac_f32_e32 v104, v160, v224
	v_fmac_f32_e32 v105, v161, v225
	v_fmac_f32_e32 v104, v162, v226
	v_fmac_f32_e32 v105, v163, v227
	v_fmac_f32_e32 v104, v164, v228
	v_fmac_f32_e32 v105, v165, v229
	v_fmac_f32_e32 v104, v166, v230
	v_fmac_f32_e32 v105, v167, v231
	v_add_f32_e32 v232, v104, v105
	s_waitcnt lgkmcnt(0)
	ds_read_b128 v[136:139], v9 offset:544
	ds_read_b128 v[140:143], v9 offset:560
	ds_read_b128 v[144:147], v9 offset:576
	ds_read_b128 v[148:151], v9 offset:592
	ds_read_b128 v[152:155], v9 offset:608
	ds_read_b128 v[156:159], v9 offset:624
	ds_read_b128 v[160:163], v9 offset:640
	ds_read_b128 v[164:167], v9 offset:656
	v_mul_f32_e32 v104, v168, v200
	v_mul_f32_e32 v105, v169, v201
	v_fmac_f32_e32 v104, v170, v202
	v_fmac_f32_e32 v105, v171, v203
	v_fmac_f32_e32 v104, v172, v204
	v_fmac_f32_e32 v105, v173, v205
	v_fmac_f32_e32 v104, v174, v206
	v_fmac_f32_e32 v105, v175, v207
	v_fmac_f32_e32 v104, v176, v208
	v_fmac_f32_e32 v105, v177, v209
	v_fmac_f32_e32 v104, v178, v210
	v_fmac_f32_e32 v105, v179, v211
	v_fmac_f32_e32 v104, v180, v212
	v_fmac_f32_e32 v105, v181, v213
	v_fmac_f32_e32 v104, v182, v214
	v_fmac_f32_e32 v105, v183, v215
	v_fmac_f32_e32 v104, v184, v216
	v_fmac_f32_e32 v105, v185, v217
	v_fmac_f32_e32 v104, v186, v218
	v_fmac_f32_e32 v105, v187, v219
	v_fmac_f32_e32 v104, v188, v220
	v_fmac_f32_e32 v105, v189, v221
	v_fmac_f32_e32 v104, v190, v222
	v_fmac_f32_e32 v105, v191, v223
	v_fmac_f32_e32 v104, v192, v224
	v_fmac_f32_e32 v105, v193, v225
	v_fmac_f32_e32 v104, v194, v226
	v_fmac_f32_e32 v105, v195, v227
	v_fmac_f32_e32 v104, v196, v228
	v_fmac_f32_e32 v105, v197, v229
	v_fmac_f32_e32 v104, v198, v230
	v_fmac_f32_e32 v105, v199, v231
	v_add_f32_e32 v233, v104, v105
	s_waitcnt lgkmcnt(0)
	ds_read_b128 v[168:171], v9 offset:816
	ds_read_b128 v[172:175], v9 offset:832
	ds_read_b128 v[176:179], v9 offset:848
	ds_read_b128 v[180:183], v9 offset:864
	ds_read_b128 v[184:187], v9 offset:880
	ds_read_b128 v[188:191], v9 offset:896
	ds_read_b128 v[192:195], v9 offset:912
	ds_read_b128 v[196:199], v9 offset:928
	v_mul_f32_e32 v104, v136, v200
	v_mul_f32_e32 v105, v137, v201
	v_fmac_f32_e32 v104, v138, v202
	v_fmac_f32_e32 v105, v139, v203
	v_fmac_f32_e32 v104, v140, v204
	v_fmac_f32_e32 v105, v141, v205
	v_fmac_f32_e32 v104, v142, v206
	v_fmac_f32_e32 v105, v143, v207
	v_fmac_f32_e32 v104, v144, v208
	v_fmac_f32_e32 v105, v145, v209
	v_fmac_f32_e32 v104, v146, v210
	v_fmac_f32_e32 v105, v147, v211
	v_fmac_f32_e32 v104, v148, v212
	v_fmac_f32_e32 v105, v149, v213
	v_fmac_f32_e32 v104, v150, v214
	v_fmac_f32_e32 v105, v151, v215
	v_fmac_f32_e32 v104, v152, v216
	v_fmac_f32_e32 v105, v153, v217
	v_fmac_f32_e32 v104, v154, v218
	v_fmac_f32_e32 v105, v155, v219
	v_fmac_f32_e32 v104, v156, v220
	v_fmac_f32_e32 v105, v157, v221
	v_fmac_f32_e32 v104, v158, v222
	v_fmac_f32_e32 v105, v159, v223
	v_fmac_f32_e32 v104, v160, v224
	v_fmac_f32_e32 v105, v161, v225
	v_fmac_f32_e32 v104, v162, v226
	v_fmac_f32_e32 v105, v163, v227
	v_fmac_f32_e32 v104, v164, v228
	v_fmac_f32_e32 v105, v165, v229
	v_fmac_f32_e32 v104, v166, v230
	v_fmac_f32_e32 v105, v167, v231
	v_add_f32_e32 v234, v104, v105
	s_waitcnt lgkmcnt(0)
	v_mul_f32_e32 v104, v168, v200
	v_mul_f32_e32 v105, v169, v201
	v_fmac_f32_e32 v104, v170, v202
	v_fmac_f32_e32 v105, v171, v203
	v_fmac_f32_e32 v104, v172, v204
	v_fmac_f32_e32 v105, v173, v205
	v_fmac_f32_e32 v104, v174, v206
	v_fmac_f32_e32 v105, v175, v207
	v_fmac_f32_e32 v104, v176, v208
	v_fmac_f32_e32 v105, v177, v209
	v_fmac_f32_e32 v104, v178, v210
	v_fmac_f32_e32 v105, v179, v211
	v_fmac_f32_e32 v104, v180, v212
	v_fmac_f32_e32 v105, v181, v213
	v_fmac_f32_e32 v104, v182, v214
	v_fmac_f32_e32 v105, v183, v215
	v_fmac_f32_e32 v104, v184, v216
	v_fmac_f32_e32 v105, v185, v217
	v_fmac_f32_e32 v104, v186, v218
	v_fmac_f32_e32 v105, v187, v219
	v_fmac_f32_e32 v104, v188, v220
	v_fmac_f32_e32 v105, v189, v221
	v_fmac_f32_e32 v104, v190, v222
	v_fmac_f32_e32 v105, v191, v223
	v_fmac_f32_e32 v104, v192, v224
	v_fmac_f32_e32 v105, v193, v225
	v_fmac_f32_e32 v104, v194, v226
	v_fmac_f32_e32 v105, v195, v227
	v_fmac_f32_e32 v104, v196, v228
	v_fmac_f32_e32 v105, v197, v229
	v_fmac_f32_e32 v104, v198, v230
	v_fmac_f32_e32 v105, v199, v231
	v_add_f32_e32 v235, v104, v105
	ds_write_b32 v10, v232 offset:8192
	ds_write_b32 v10, v233 offset:8320
	ds_write_b32 v10, v234 offset:8448
	ds_write_b32 v10, v235 offset:8576
	s_waitcnt lgkmcnt(0)
	s_barrier
	ds_read_b32 v200, v8 offset:8192
	ds_read_b32 v201, v8 offset:8320
	ds_read_b32 v202, v8 offset:8448
	ds_read_b32 v203, v8 offset:8576
	ds_read_b32 v204, v8 offset:8704
	ds_read_b32 v205, v8 offset:8832
	ds_read_b32 v206, v8 offset:8960
	ds_read_b32 v207, v8 offset:9088
	ds_read_b32 v208, v8 offset:9216
	ds_read_b32 v209, v8 offset:9344
	ds_read_b32 v210, v8 offset:9472
	ds_read_b32 v211, v8 offset:9600
	ds_read_b32 v212, v8 offset:9728
	ds_read_b32 v213, v8 offset:9856
	ds_read_b32 v214, v8 offset:9984
	ds_read_b32 v215, v8 offset:10112
	ds_read_b32 v216, v8 offset:10240
	ds_read_b32 v217, v8 offset:10368
	ds_read_b32 v218, v8 offset:10496
	ds_read_b32 v219, v8 offset:10624
	ds_read_b32 v220, v8 offset:10752
	ds_read_b32 v221, v8 offset:10880
	ds_read_b32 v222, v8 offset:11008
	ds_read_b32 v223, v8 offset:11136
	ds_read_b32 v224, v8 offset:11264
	ds_read_b32 v225, v8 offset:11392
	ds_read_b32 v226, v8 offset:11520
	ds_read_b32 v227, v8 offset:11648
	ds_read_b32 v228, v8 offset:11776
	ds_read_b32 v229, v8 offset:11904
	ds_read_b32 v230, v8 offset:12032
	ds_read_b32 v231, v8 offset:12160
	ds_read_b128 v[136:139], v11 offset:4096
	ds_read_b128 v[140:143], v11 offset:4112
	ds_read_b128 v[144:147], v11 offset:4128
	ds_read_b128 v[148:151], v11 offset:4144
	ds_read_b128 v[152:155], v11 offset:4160
	ds_read_b128 v[156:159], v11 offset:4176
	ds_read_b128 v[160:163], v11 offset:4192
	ds_read_b128 v[164:167], v11 offset:4208
	s_waitcnt lgkmcnt(0)
	ds_read_b128 v[168:171], v11 offset:4224
	ds_read_b128 v[172:175], v11 offset:4240
	ds_read_b128 v[176:179], v11 offset:4256
	ds_read_b128 v[180:183], v11 offset:4272
	ds_read_b128 v[184:187], v11 offset:4288
	ds_read_b128 v[188:191], v11 offset:4304
	ds_read_b128 v[192:195], v11 offset:4320
	ds_read_b128 v[196:199], v11 offset:4336
	v_mul_f32_e32 v104, v136, v200
	v_mul_f32_e32 v105, v137, v201
	v_fmac_f32_e32 v104, v138, v202
	v_fmac_f32_e32 v105, v139, v203
	v_fmac_f32_e32 v104, v140, v204
	v_fmac_f32_e32 v105, v141, v205
	v_fmac_f32_e32 v104, v142, v206
	v_fmac_f32_e32 v105, v143, v207
	v_fmac_f32_e32 v104, v144, v208
	v_fmac_f32_e32 v105, v145, v209
	v_fmac_f32_e32 v104, v146, v210
	v_fmac_f32_e32 v105, v147, v211
	v_fmac_f32_e32 v104, v148, v212
	v_fmac_f32_e32 v105, v149, v213
	v_fmac_f32_e32 v104, v150, v214
	v_fmac_f32_e32 v105, v151, v215
	v_fmac_f32_e32 v104, v152, v216
	v_fmac_f32_e32 v105, v153, v217
	v_fmac_f32_e32 v104, v154, v218
	v_fmac_f32_e32 v105, v155, v219
	v_fmac_f32_e32 v104, v156, v220
	v_fmac_f32_e32 v105, v157, v221
	v_fmac_f32_e32 v104, v158, v222
	v_fmac_f32_e32 v105, v159, v223
	v_fmac_f32_e32 v104, v160, v224
	v_fmac_f32_e32 v105, v161, v225
	v_fmac_f32_e32 v104, v162, v226
	v_fmac_f32_e32 v105, v163, v227
	v_fmac_f32_e32 v104, v164, v228
	v_fmac_f32_e32 v105, v165, v229
	v_fmac_f32_e32 v104, v166, v230
	v_fmac_f32_e32 v105, v167, v231
	v_add_f32_e32 v232, v104, v105
	s_waitcnt lgkmcnt(0)
	ds_read_b128 v[136:139], v11 offset:4352
	ds_read_b128 v[140:143], v11 offset:4368
	ds_read_b128 v[144:147], v11 offset:4384
	ds_read_b128 v[148:151], v11 offset:4400
	ds_read_b128 v[152:155], v11 offset:4416
	ds_read_b128 v[156:159], v11 offset:4432
	ds_read_b128 v[160:163], v11 offset:4448
	ds_read_b128 v[164:167], v11 offset:4464
	v_mul_f32_e32 v104, v168, v200
	v_mul_f32_e32 v105, v169, v201
	v_fmac_f32_e32 v104, v170, v202
	v_fmac_f32_e32 v105, v171, v203
	v_fmac_f32_e32 v104, v172, v204
	v_fmac_f32_e32 v105, v173, v205
	v_fmac_f32_e32 v104, v174, v206
	v_fmac_f32_e32 v105, v175, v207
	v_fmac_f32_e32 v104, v176, v208
	v_fmac_f32_e32 v105, v177, v209
	v_fmac_f32_e32 v104, v178, v210
	v_fmac_f32_e32 v105, v179, v211
	v_fmac_f32_e32 v104, v180, v212
	v_fmac_f32_e32 v105, v181, v213
	v_fmac_f32_e32 v104, v182, v214
	v_fmac_f32_e32 v105, v183, v215
	v_fmac_f32_e32 v104, v184, v216
	v_fmac_f32_e32 v105, v185, v217
	v_fmac_f32_e32 v104, v186, v218
	v_fmac_f32_e32 v105, v187, v219
	v_fmac_f32_e32 v104, v188, v220
	v_fmac_f32_e32 v105, v189, v221
	v_fmac_f32_e32 v104, v190, v222
	v_fmac_f32_e32 v105, v191, v223
	v_fmac_f32_e32 v104, v192, v224
	v_fmac_f32_e32 v105, v193, v225
	v_fmac_f32_e32 v104, v194, v226
	v_fmac_f32_e32 v105, v195, v227
	v_fmac_f32_e32 v104, v196, v228
	v_fmac_f32_e32 v105, v197, v229
	v_fmac_f32_e32 v104, v198, v230
	v_fmac_f32_e32 v105, v199, v231
	v_add_f32_e32 v233, v104, v105
	s_waitcnt lgkmcnt(0)
	ds_read_b128 v[168:171], v11 offset:4480
	ds_read_b128 v[172:175], v11 offset:4496
	ds_read_b128 v[176:179], v11 offset:4512
	ds_read_b128 v[180:183], v11 offset:4528
	ds_read_b128 v[184:187], v11 offset:4544
	ds_read_b128 v[188:191], v11 offset:4560
	ds_read_b128 v[192:195], v11 offset:4576
	ds_read_b128 v[196:199], v11 offset:4592
	v_mul_f32_e32 v104, v136, v200
	v_mul_f32_e32 v105, v137, v201
	v_fmac_f32_e32 v104, v138, v202
	v_fmac_f32_e32 v105, v139, v203
	v_fmac_f32_e32 v104, v140, v204
	v_fmac_f32_e32 v105, v141, v205
	v_fmac_f32_e32 v104, v142, v206
	v_fmac_f32_e32 v105, v143, v207
	v_fmac_f32_e32 v104, v144, v208
	v_fmac_f32_e32 v105, v145, v209
	v_fmac_f32_e32 v104, v146, v210
	v_fmac_f32_e32 v105, v147, v211
	v_fmac_f32_e32 v104, v148, v212
	v_fmac_f32_e32 v105, v149, v213
	v_fmac_f32_e32 v104, v150, v214
	v_fmac_f32_e32 v105, v151, v215
	v_fmac_f32_e32 v104, v152, v216
	v_fmac_f32_e32 v105, v153, v217
	v_fmac_f32_e32 v104, v154, v218
	v_fmac_f32_e32 v105, v155, v219
	v_fmac_f32_e32 v104, v156, v220
	v_fmac_f32_e32 v105, v157, v221
	v_fmac_f32_e32 v104, v158, v222
	v_fmac_f32_e32 v105, v159, v223
	v_fmac_f32_e32 v104, v160, v224
	v_fmac_f32_e32 v105, v161, v225
	v_fmac_f32_e32 v104, v162, v226
	v_fmac_f32_e32 v105, v163, v227
	v_fmac_f32_e32 v104, v164, v228
	v_fmac_f32_e32 v105, v165, v229
	v_fmac_f32_e32 v104, v166, v230
	v_fmac_f32_e32 v105, v167, v231
	v_add_f32_e32 v234, v104, v105
	s_waitcnt lgkmcnt(0)
	v_mul_f32_e32 v104, v168, v200
	v_mul_f32_e32 v105, v169, v201
	v_fmac_f32_e32 v104, v170, v202
	v_fmac_f32_e32 v105, v171, v203
	v_fmac_f32_e32 v104, v172, v204
	v_fmac_f32_e32 v105, v173, v205
	v_fmac_f32_e32 v104, v174, v206
	v_fmac_f32_e32 v105, v175, v207
	v_fmac_f32_e32 v104, v176, v208
	v_fmac_f32_e32 v105, v177, v209
	v_fmac_f32_e32 v104, v178, v210
	v_fmac_f32_e32 v105, v179, v211
	v_fmac_f32_e32 v104, v180, v212
	v_fmac_f32_e32 v105, v181, v213
	v_fmac_f32_e32 v104, v182, v214
	v_fmac_f32_e32 v105, v183, v215
	v_fmac_f32_e32 v104, v184, v216
	v_fmac_f32_e32 v105, v185, v217
	v_fmac_f32_e32 v104, v186, v218
	v_fmac_f32_e32 v105, v187, v219
	v_fmac_f32_e32 v104, v188, v220
	v_fmac_f32_e32 v105, v189, v221
	v_fmac_f32_e32 v104, v190, v222
	v_fmac_f32_e32 v105, v191, v223
	v_fmac_f32_e32 v104, v192, v224
	v_fmac_f32_e32 v105, v193, v225
	v_fmac_f32_e32 v104, v194, v226
	v_fmac_f32_e32 v105, v195, v227
	v_fmac_f32_e32 v104, v196, v228
	v_fmac_f32_e32 v105, v197, v229
	v_fmac_f32_e32 v104, v198, v230
	v_fmac_f32_e32 v105, v199, v231
	v_add_f32_e32 v235, v104, v105
	s_lshl_b32 s24, s1, 8
	s_add_i32 s24, s24, 0x23200
	v_add3_u32 v12, v61, v5, s24
	ds_read_b32 v13, v12
	ds_read_b32 v14, v12 offset:512
	v_mul_u32_u24_e32 v15, 0x240, v4
	s_add_i32 s24, s13, 0x1200
	v_lshl_add_u32 v15, v108, 1, v15
	v_add3_u32 v15, v61, v15, s24
	s_waitcnt lgkmcnt(0)
	v_mul_f32_e32 v13, 0x3fb8aa3b, v13
	v_exp_f32_e32 v13, v13
	s_nop 0
	v_mul_f32_e32 v13, v14, v13
	v_mul_f32_e64 v16, -v232, v13
	v_mul_f32_e64 v17, -v232, v14
	v_cvt_pk_bf16_f32 v16, v16, v16
	v_cvt_pk_bf16_f32 v17, v17, v17
	ds_write_b16 v15, v16 offset:0
	ds_write_b16 v15, v17 offset:9216
	v_mul_f32_e64 v16, -v233, v13
	v_mul_f32_e64 v17, -v233, v14
	v_cvt_pk_bf16_f32 v16, v16, v16
	v_cvt_pk_bf16_f32 v17, v17, v17
	ds_write_b16 v15, v16 offset:144
	ds_write_b16 v15, v17 offset:9360
	v_mul_f32_e64 v16, -v234, v13
	v_mul_f32_e64 v17, -v234, v14
	v_cvt_pk_bf16_f32 v16, v16, v16
	v_cvt_pk_bf16_f32 v17, v17, v17
	ds_write_b16 v15, v16 offset:288
	ds_write_b16 v15, v17 offset:9504
	v_mul_f32_e64 v16, -v235, v13
	v_mul_f32_e64 v17, -v235, v14
	v_cvt_pk_bf16_f32 v16, v16, v16
	v_cvt_pk_bf16_f32 v17, v17, v17
	ds_write_b16 v15, v16 offset:432
	ds_write_b16 v15, v17 offset:9648
	s_cmp_gt_u32 s10, 1
	s_cbranch_scc1 .Lg4_done
	s_lshl_b32 s24, s10, 8
	v_lshlrev_b32_e32 v5, 2, v21
	s_add_i32 s24, s24, 0x23200
	v_lshrrev_b32_e32 v4, 5, v21
	v_add3_u32 v12, v61, v5, s24
	ds_read_b32 v13, v12
	ds_read_b32 v14, v12 offset:512
	v_mul_u32_u24_e32 v6, 0x1200, v4
	s_mul_i32 s24, s10, 0x4800
	v_lshl_add_u32 v6, v21, 1, v6
	v_add3_u32 v15, v61, v6, s24
	s_waitcnt lgkmcnt(0)
	v_mul_f32_e32 v13, 0x3fb8aa3b, v13
	v_exp_f32_e32 v13, v13
	s_nop 0
	v_mul_f32_e32 v13, v14, v13
	v_mul_f32_e32 v16, v72, v13
	v_mul_f32_e32 v17, v72, v14
	v_cvt_pk_bf16_f32 v16, v16, v16
	v_cvt_pk_bf16_f32 v17, v17, v17
	ds_write_b16 v15, v16 offset:0
	ds_write_b16 v15, v17 offset:9216
	v_mul_f32_e32 v16, v73, v13
	v_mul_f32_e32 v17, v73, v14
	v_cvt_pk_bf16_f32 v16, v16, v16
	v_cvt_pk_bf16_f32 v17, v17, v17
	ds_write_b16 v15, v16 offset:144
	ds_write_b16 v15, v17 offset:9360
	v_mul_f32_e32 v16, v74, v13
	v_mul_f32_e32 v17, v74, v14
	v_cvt_pk_bf16_f32 v16, v16, v16
	v_cvt_pk_bf16_f32 v17, v17, v17
	ds_write_b16 v15, v16 offset:288
	ds_write_b16 v15, v17 offset:9504
	v_mul_f32_e32 v16, v75, v13
	v_mul_f32_e32 v17, v75, v14
	v_cvt_pk_bf16_f32 v16, v16, v16
	v_cvt_pk_bf16_f32 v17, v17, v17
	ds_write_b16 v15, v16 offset:432
	ds_write_b16 v15, v17 offset:9648
	v_mul_f32_e32 v16, v76, v13
	v_mul_f32_e32 v17, v76, v14
	v_cvt_pk_bf16_f32 v16, v16, v16
	v_cvt_pk_bf16_f32 v17, v17, v17
	ds_write_b16 v15, v16 offset:576
	ds_write_b16 v15, v17 offset:9792
	v_mul_f32_e32 v16, v77, v13
	v_mul_f32_e32 v17, v77, v14
	v_cvt_pk_bf16_f32 v16, v16, v16
	v_cvt_pk_bf16_f32 v17, v17, v17
	ds_write_b16 v15, v16 offset:720
	ds_write_b16 v15, v17 offset:9936
	v_mul_f32_e32 v16, v78, v13
	v_mul_f32_e32 v17, v78, v14
	v_cvt_pk_bf16_f32 v16, v16, v16
	v_cvt_pk_bf16_f32 v17, v17, v17
	ds_write_b16 v15, v16 offset:864
	ds_write_b16 v15, v17 offset:10080
	v_mul_f32_e32 v16, v79, v13
	v_mul_f32_e32 v17, v79, v14
	v_cvt_pk_bf16_f32 v16, v16, v16
	v_cvt_pk_bf16_f32 v17, v17, v17
	ds_write_b16 v15, v16 offset:1008
	ds_write_b16 v15, v17 offset:10224
	v_mul_f32_e32 v16, v80, v13
	v_mul_f32_e32 v17, v80, v14
	v_cvt_pk_bf16_f32 v16, v16, v16
	v_cvt_pk_bf16_f32 v17, v17, v17
	ds_write_b16 v15, v16 offset:1152
	ds_write_b16 v15, v17 offset:10368
	v_mul_f32_e32 v16, v81, v13
	v_mul_f32_e32 v17, v81, v14
	v_cvt_pk_bf16_f32 v16, v16, v16
	v_cvt_pk_bf16_f32 v17, v17, v17
	ds_write_b16 v15, v16 offset:1296
	ds_write_b16 v15, v17 offset:10512
	v_mul_f32_e32 v16, v82, v13
	v_mul_f32_e32 v17, v82, v14
	v_cvt_pk_bf16_f32 v16, v16, v16
	v_cvt_pk_bf16_f32 v17, v17, v17
	ds_write_b16 v15, v16 offset:1440
	ds_write_b16 v15, v17 offset:10656
	v_mul_f32_e32 v16, v83, v13
	v_mul_f32_e32 v17, v83, v14
	v_cvt_pk_bf16_f32 v16, v16, v16
	v_cvt_pk_bf16_f32 v17, v17, v17
	ds_write_b16 v15, v16 offset:1584
	ds_write_b16 v15, v17 offset:10800
	v_mul_f32_e32 v16, v84, v13
	v_mul_f32_e32 v17, v84, v14
	v_cvt_pk_bf16_f32 v16, v16, v16
	v_cvt_pk_bf16_f32 v17, v17, v17
	ds_write_b16 v15, v16 offset:1728
	ds_write_b16 v15, v17 offset:10944
	v_mul_f32_e32 v16, v85, v13
	v_mul_f32_e32 v17, v85, v14
	v_cvt_pk_bf16_f32 v16, v16, v16
	v_cvt_pk_bf16_f32 v17, v17, v17
	ds_write_b16 v15, v16 offset:1872
	ds_write_b16 v15, v17 offset:11088
	v_mul_f32_e32 v16, v86, v13
	v_mul_f32_e32 v17, v86, v14
	v_cvt_pk_bf16_f32 v16, v16, v16
	v_cvt_pk_bf16_f32 v17, v17, v17
	ds_write_b16 v15, v16 offset:2016
	ds_write_b16 v15, v17 offset:11232
	v_mul_f32_e32 v16, v87, v13
	v_mul_f32_e32 v17, v87, v14
	v_cvt_pk_bf16_f32 v16, v16, v16
	v_cvt_pk_bf16_f32 v17, v17, v17
	ds_write_b16 v15, v16 offset:2160
	ds_write_b16 v15, v17 offset:11376
	v_mul_f32_e32 v16, v88, v13
	v_mul_f32_e32 v17, v88, v14
	v_cvt_pk_bf16_f32 v16, v16, v16
	v_cvt_pk_bf16_f32 v17, v17, v17
	ds_write_b16 v15, v16 offset:2304
	ds_write_b16 v15, v17 offset:11520
	v_mul_f32_e32 v16, v89, v13
	v_mul_f32_e32 v17, v89, v14
	v_cvt_pk_bf16_f32 v16, v16, v16
	v_cvt_pk_bf16_f32 v17, v17, v17
	ds_write_b16 v15, v16 offset:2448
	ds_write_b16 v15, v17 offset:11664
	v_mul_f32_e32 v16, v90, v13
	v_mul_f32_e32 v17, v90, v14
	v_cvt_pk_bf16_f32 v16, v16, v16
	v_cvt_pk_bf16_f32 v17, v17, v17
	ds_write_b16 v15, v16 offset:2592
	ds_write_b16 v15, v17 offset:11808
	v_mul_f32_e32 v16, v91, v13
	v_mul_f32_e32 v17, v91, v14
	v_cvt_pk_bf16_f32 v16, v16, v16
	v_cvt_pk_bf16_f32 v17, v17, v17
	ds_write_b16 v15, v16 offset:2736
	ds_write_b16 v15, v17 offset:11952
	v_mul_f32_e32 v16, v92, v13
	v_mul_f32_e32 v17, v92, v14
	v_cvt_pk_bf16_f32 v16, v16, v16
	v_cvt_pk_bf16_f32 v17, v17, v17
	ds_write_b16 v15, v16 offset:2880
	ds_write_b16 v15, v17 offset:12096
	v_mul_f32_e32 v16, v93, v13
	v_mul_f32_e32 v17, v93, v14
	v_cvt_pk_bf16_f32 v16, v16, v16
	v_cvt_pk_bf16_f32 v17, v17, v17
	ds_write_b16 v15, v16 offset:3024
	ds_write_b16 v15, v17 offset:12240
	v_mul_f32_e32 v16, v94, v13
	v_mul_f32_e32 v17, v94, v14
	v_cvt_pk_bf16_f32 v16, v16, v16
	v_cvt_pk_bf16_f32 v17, v17, v17
	ds_write_b16 v15, v16 offset:3168
	ds_write_b16 v15, v17 offset:12384
	v_mul_f32_e32 v16, v95, v13
	v_mul_f32_e32 v17, v95, v14
	v_cvt_pk_bf16_f32 v16, v16, v16
	v_cvt_pk_bf16_f32 v17, v17, v17
	ds_write_b16 v15, v16 offset:3312
	ds_write_b16 v15, v17 offset:12528
	v_mul_f32_e32 v16, v96, v13
	v_mul_f32_e32 v17, v96, v14
	v_cvt_pk_bf16_f32 v16, v16, v16
	v_cvt_pk_bf16_f32 v17, v17, v17
	ds_write_b16 v15, v16 offset:3456
	ds_write_b16 v15, v17 offset:12672
	v_mul_f32_e32 v16, v97, v13
	v_mul_f32_e32 v17, v97, v14
	v_cvt_pk_bf16_f32 v16, v16, v16
	v_cvt_pk_bf16_f32 v17, v17, v17
	ds_write_b16 v15, v16 offset:3600
	ds_write_b16 v15, v17 offset:12816
	v_mul_f32_e32 v16, v98, v13
	v_mul_f32_e32 v17, v98, v14
	v_cvt_pk_bf16_f32 v16, v16, v16
	v_cvt_pk_bf16_f32 v17, v17, v17
	ds_write_b16 v15, v16 offset:3744
	ds_write_b16 v15, v17 offset:12960
	v_mul_f32_e32 v16, v99, v13
	v_mul_f32_e32 v17, v99, v14
	v_cvt_pk_bf16_f32 v16, v16, v16
	v_cvt_pk_bf16_f32 v17, v17, v17
	ds_write_b16 v15, v16 offset:3888
	ds_write_b16 v15, v17 offset:13104
	v_mul_f32_e32 v16, v100, v13
	v_mul_f32_e32 v17, v100, v14
	v_cvt_pk_bf16_f32 v16, v16, v16
	v_cvt_pk_bf16_f32 v17, v17, v17
	ds_write_b16 v15, v16 offset:4032
	ds_write_b16 v15, v17 offset:13248
	v_mul_f32_e32 v16, v101, v13
	v_mul_f32_e32 v17, v101, v14
	v_cvt_pk_bf16_f32 v16, v16, v16
	v_cvt_pk_bf16_f32 v17, v17, v17
	ds_write_b16 v15, v16 offset:4176
	ds_write_b16 v15, v17 offset:13392
	v_mul_f32_e32 v16, v102, v13
	v_mul_f32_e32 v17, v102, v14
	v_cvt_pk_bf16_f32 v16, v16, v16
	v_cvt_pk_bf16_f32 v17, v17, v17
	ds_write_b16 v15, v16 offset:4320
	ds_write_b16 v15, v17 offset:13536
	v_mul_f32_e32 v16, v103, v13
	v_mul_f32_e32 v17, v103, v14
	v_cvt_pk_bf16_f32 v16, v16, v16
	v_cvt_pk_bf16_f32 v17, v17, v17
	ds_write_b16 v15, v16 offset:4464
	ds_write_b16 v15, v17 offset:13680
	v_lshrrev_b32_e32 v18, 3, v21
	v_and_b32_e32 v19, 7, v21
	v_mul_u32_u24_e32 v18, 0x90, v18
	s_mul_i32 s24, s10, 0x4800
	v_lshl_add_u32 v18, v19, 3, v18
	v_mov_b32_e32 v16, 0
	v_add3_u32 v18, v61, v18, s24
	v_mov_b32_e32 v17, 0
	ds_write_b64 v18, v[16:17] offset:64
	ds_write_b64 v18, v[16:17] offset:9280
	ds_write_b64 v18, v[16:17] offset:1216
	ds_write_b64 v18, v[16:17] offset:10432
	ds_write_b64 v18, v[16:17] offset:2368
	ds_write_b64 v18, v[16:17] offset:11584
	ds_write_b64 v18, v[16:17] offset:3520
	ds_write_b64 v18, v[16:17] offset:12736
